# bias-init LDS reads moved further to the loop top behind the first two layer-0 MFMAs (off the reduce path entirely)
# baseline (speedup 1.0000x reference)
.LBB1_2:
	v_lshrrev_b32_e32 v151, 4, v137
	s_lshl_b64 s[6:7], s[2:3], 4
	v_cmp_eq_u32_e64 s[2:3], 1, v151
	s_waitcnt vmcnt(31)
	v_cvt_f16_f32_e32 v8, v8
	v_cmp_gt_u32_e32 vcc, 16, v137
	s_waitcnt vmcnt(29)
	v_cndmask_b32_e64 v116, 0, v116, s[2:3]
	s_waitcnt vmcnt(21)
	v_cndmask_b32_e64 v100, 0, v100, s[2:3]
	v_cmp_eq_u32_e64 s[0:1], 2, v151
	v_cndmask_b32_e64 v114, 0, v114, s[2:3]
	v_cndmask_b32_e64 v115, 0, v115, s[2:3]
	v_cndmask_b32_e32 v6, v116, v6, vcc
	v_cndmask_b32_e64 v116, 0, v117, s[2:3]
	v_cndmask_b32_e64 v108, 0, v108, s[2:3]
	v_cndmask_b32_e32 v26, v100, v26, vcc
	v_cvt_f16_f32_e32 v29, v29
	v_cndmask_b32_e64 v100, 0, v101, s[2:3]
	v_cndmask_b32_e32 v28, 0, v28, vcc
	v_cndmask_b32_e64 v152, 0, 1.0, s[0:1]
	v_cndmask_b32_e32 v114, v114, v120, vcc
	v_cndmask_b32_e32 v115, v115, v121, vcc
	v_cndmask_b32_e32 v7, v116, v7, vcc
	v_cndmask_b32_e64 v106, 0, v106, s[2:3]
	v_cndmask_b32_e64 v107, 0, v107, s[2:3]
	v_cndmask_b32_e32 v14, v108, v14, vcc
	v_cndmask_b32_e64 v108, 0, v109, s[2:3]
	v_cndmask_b32_e32 v27, v100, v27, vcc
	v_cvt_f16_f32_e32 v100, v28
	v_cndmask_b32_e32 v116, 0, v8, vcc
	v_cvt_pk_f16_f32 v8, v6, v7
	v_cvt_pk_f16_f32 v7, v114, v115
	v_cndmask_b32_e64 v114, v152, v140, s[2:3]
	v_cndmask_b32_e32 v106, v106, v112, vcc
	v_cndmask_b32_e32 v107, v107, v113, vcc
	v_cndmask_b32_e32 v15, v108, v15, vcc
	v_cndmask_b32_e64 v98, 0, v98, s[2:3]
	v_cndmask_b32_e64 v99, 0, v99, s[2:3]
	v_cndmask_b32_e32 v110, v114, v110, vcc
	v_cndmask_b32_e64 v114, 0, v141, s[2:3]
	v_cndmask_b32_e32 v108, 0, v16, vcc
	v_cvt_pk_f16_f32 v16, v14, v15
	v_cvt_pk_f16_f32 v15, v106, v107
	v_cndmask_b32_e64 v106, v152, v138, s[2:3]
	v_cndmask_b32_e32 v98, v98, v104, vcc
	v_cndmask_b32_e32 v99, v99, v105, vcc
	v_cndmask_b32_e32 v111, v114, v111, vcc
	v_cndmask_b32_e32 v102, v106, v102, vcc
	v_cndmask_b32_e64 v106, 0, v139, s[2:3]
	v_cndmask_b32_e32 v29, 0, v29, vcc
	v_cvt_pk_f16_f32 v28, v26, v27
	v_cvt_pk_f16_f32 v27, v98, v99
	v_lshlrev_b32_e32 v101, 10, v1
	v_bitop3_b32 v98, v151, v0, 3 bitop3:0x78
	v_lshl_add_u64 v[130:131], s[4:5], 0, v[130:131]
	v_cvt_f16_f32_e32 v4, v4
	v_cvt_pk_f16_f32 v14, v110, v111
	v_cndmask_b32_e32 v103, v106, v103, vcc
	v_pack_b32_f16 v29, v100, v29
	v_lshl_or_b32 v111, v98, 4, v101
	v_lshlrev_b32_e32 v100, 4, v1
	s_movk_i32 s4, 0xc0
	v_cndmask_b32_e64 v124, 0, v124, s[2:3]
	v_cvt_pk_f16_f32 v26, v102, v103
	v_and_b32_e32 v112, 0xc0, v100
	v_bitop3_b32 v100, v100, s4, v111 bitop3:0x26
	s_lshl_b32 s4, s20, 3
	v_lshrrev_b32_e32 v102, 5, v137
	v_lshrrev_b32_e32 v104, 1, v137
	v_cndmask_b32_e64 v122, 0, v122, s[2:3]
	v_cndmask_b32_e64 v123, 0, v123, s[2:3]
	v_cndmask_b32_e32 v2, v124, v2, vcc
	v_cvt_f16_f32_e32 v5, v5
	v_cndmask_b32_e64 v124, 0, v125, s[2:3]
	v_cvt_f16_f32_e32 v9, v9
	v_or_b32_e32 v103, s4, v102
	v_and_or_b32 v110, v104, 8, v101
	v_bitop3_b32 v101, s4, v1, v102 bitop3:0x36
	s_lshl_b32 s4, s20, 4
	v_cndmask_b32_e32 v122, v122, v128, vcc
	v_cndmask_b32_e32 v123, v123, v129, vcc
	v_cndmask_b32_e32 v3, v124, v3, vcc
	v_cndmask_b32_e32 v17, 0, v17, vcc
	v_lshlrev_b32_e32 v107, 4, v101
	v_bitop3_b32 v101, v103, v1, 2 bitop3:0x36
	s_add_i32 s4, s4, 0x10000
	v_bfe_u32 v0, v0, 4, 2
	v_cndmask_b32_e64 v144, v152, v144, s[2:3]
	v_cndmask_b32_e32 v124, 0, v4, vcc
	v_cvt_pk_f16_f32 v4, v2, v3
	v_cvt_pk_f16_f32 v3, v122, v123
	v_cndmask_b32_e64 v122, v152, v142, s[2:3]
	v_cvt_pk_f16_f32 v17, v108, v17
	s_movk_i32 s5, 0x80
	v_lshlrev_b32_e32 v108, 4, v101
	v_bitop3_b32 v101, v103, v1, 4 bitop3:0x36
	s_cmp_lt_u32 s22, 64
	v_lshlrev_b32_e32 v104, 5, v0
	v_lshlrev_b32_e32 v0, 6, v0
	v_cndmask_b32_e32 v126, v144, v126, vcc
	v_cndmask_b32_e64 v144, 0, v145, s[2:3]
	v_cndmask_b32_e32 v118, v122, v118, vcc
	v_cndmask_b32_e64 v122, 0, v143, s[2:3]
	v_bitop3_b32 v99, v112, s5, v111 bitop3:0x36
	v_lshlrev_b32_e32 v109, 4, v101
	v_bitop3_b32 v101, v103, v1, 6 bitop3:0x36
	v_lshl_or_b32 v105, s20, 8, v0
	v_mov_b32_e32 v0, 0x1ec00
	s_cselect_b64 s[4:5], -1, 0
	v_cndmask_b32_e32 v127, v144, v127, vcc
	v_cndmask_b32_e32 v5, 0, v5, vcc
	v_cndmask_b32_e32 v119, v122, v119, vcc
	v_cndmask_b32_e32 v9, 0, v9, vcc
	v_lshlrev_b32_e32 v113, 4, v101
	v_lshlrev_b32_e32 v101, 5, v1
	v_lshl_add_u32 v106, v137, 6, v0
	s_cmp_eq_u32 s20, 0
	s_cselect_b32 s31, 0, 0xffff1d00
	v_add_u32_e32 v106, s31, v106
	v_cndmask_b32_e64 v0, 0, 1, s[4:5]
	v_lshl_add_u64 v[132:133], s[8:9], 0, v[132:133]
	v_or_b32_e32 v148, 0x400, v147
	v_or_b32_e32 v149, 0x800, v147
	v_or_b32_e32 v150, 0xc00, v147
	v_cvt_pk_f16_f32 v2, v126, v127
	v_pack_b32_f16 v5, v124, v5
	v_cvt_pk_f16_f32 v6, v118, v119
	v_pack_b32_f16 v9, v116, v9
	v_bitop3_b32 v98, v112, 64, v111 bitop3:0x36
	v_lshl_or_b32 v104, s20, 7, v104
	s_mov_b32 s22, 0x98000
	s_mov_b32 s23, 0x5040100
	s_mov_b32 s24, 0x7060302
	v_add_u32_e32 v107, v107, v110
	v_add_u32_e32 v108, v108, v110
	v_add_u32_e32 v109, v109, v110
	v_add_u32_e32 v110, v113, v110
	v_add_u32_e32 v111, v112, v111
	v_lshlrev_b32_e32 v113, 4, v137
	v_or_b32_e32 v113, 0x10000, v113
	s_lshr_b32 s28, s20, 2
	s_and_b32 s29, s20, 3
	s_lshl_b32 s28, s28, 10
	s_lshl_b32 s29, s29, 2
	s_add_i32 s28, s28, s29
	v_add_u32_e32 v112, s28, v113
	v_cmp_eq_u32_e64 s[26:27], 3, v151
	v_add_u32_e32 v114, 0x12400, v101
	v_mov_b32_e32 v121, v111
	v_mov_b32_e32 v144, v98
	v_cndmask_b32_e64 v111, v111, v99, s[84:85]
	v_cndmask_b32_e64 v99, v99, v121, s[84:85]
	v_cndmask_b32_e64 v98, v98, v100, s[84:85]
	v_cndmask_b32_e64 v100, v100, v144, s[84:85]
	v_add_u32_e32 v111, s80, v111
	v_add_u32_e32 v98, s81, v98
	v_add_u32_e32 v99, s82, v99
	v_add_u32_e32 v100, s83, v100
	v_and_b32_e32 v108, 15, v137
	s_lshl_b32 s31, s20, 3
	v_add_u32_e32 v107, s31, v151
	v_xor_b32_e32 v107, v107, v108
	v_lshlrev_b32_e32 v107, 4, v107
	v_lshl_or_b32 v107, v108, 10, v107
	v_xor_b32_e32 v108, 64, v107
	v_cmp_ne_u32_e64 s[4:5], 1, v0
	s_waitcnt vmcnt(16)
	v_cndmask_b32_e64 v1, v30, v134, s[0:1]
	v_bfi_b32 v30, s10, v1, v30
	v_perm_b32 v1, v22, v134, s24
	v_cndmask_b32_e64 v22, v22, v1, s[0:1]
	v_bfi_b32 v1, s10, v135, v18
	v_perm_b32 v121, v10, v135, s24
	v_cndmask_b32_e64 v18, v18, v1, s[0:1]
	v_cndmask_b32_e64 v10, v10, v121, s[0:1]
	v_mov_b32_e32 v121, v136
	v_mov_b32_e32 v144, v136
	v_mov_b32_e32 v145, v136
	v_mov_b32_e32 v0, v136
	v_mov_b32_e32 v1, v136
	s_waitcnt lgkmcnt(0)
	s_barrier
	ds_read_u16 v102, v114
	ds_read_u16 v103, v114 offset:512
	ds_read_u16 v115, v114 offset:1024
	ds_read_u16 v116, v114 offset:1536
	v_add_u32_e32 v117, 0x12400, v105
	v_add_u32_e32 v114, 2, v114
	s_waitcnt lgkmcnt(0)
	s_branch .LBB1_4
.LBB1_4:
	s_and_saveexec_b64 s[8:9], s[2:3]
	v_perm_b32 v5, v1, v102, s23
	v_perm_b32 v9, v121, v103, s23
	s_or_b64 exec, exec, s[8:9]
	v_mov_b32_e32 v144, v1
	v_mov_b32_e32 v145, v121
	v_mfma_f32_16x16x32_f16 v[164:167], v[30:33], v[2:5], 0
	v_mfma_f32_16x16x32_f16 v[180:183], v[22:25], v[2:5], 0
	ds_read_b128 v[240:243], v117 offset:2048
	ds_read_b128 v[244:247], v117 offset:2064
	ds_read_b128 v[248:251], v117 offset:2080
	ds_read_b128 v[252:255], v117 offset:2096
	s_cmp_lg_u32 s22, 0x818000
	v_permlane32_swap_b32_e32 v1, v144
	v_permlane32_swap_b32_e32 v121, v145
	v_mfma_f32_16x16x32_f16 v[168:171], v[30:33], v[6:9], 0
	v_mfma_f32_16x16x32_f16 v[184:187], v[22:25], v[6:9], 0
	s_cselect_b32 s9, s11, 15
	s_and_saveexec_b64 s[32:33], s[2:3]
	v_perm_b32 v17, v144, v115, s23
	v_perm_b32 v29, v145, v116, s23
	s_or_b64 exec, exec, s[32:33]
	v_mfma_f32_16x16x32_f16 v[172:175], v[30:33], v[14:17], 0
	v_mfma_f32_16x16x32_f16 v[188:191], v[22:25], v[14:17], 0
	v_mfma_f32_16x16x32_f16 v[176:179], v[30:33], v[26:29], 0
	v_mfma_f32_16x16x32_f16 v[192:195], v[22:25], v[26:29], 0
	v_mfma_f32_16x16x32_f16 v[208:211], v[18:21], v[2:5], 0
	v_mfma_f32_16x16x32_f16 v[224:227], v[10:13], v[2:5], 0
	v_cvt_pk_f16_f32 v122, v164, v165
	v_cvt_pk_f16_f32 v123, v166, v167
	v_pk_max_f16 v122, v122, 0
	v_pk_max_f16 v123, v123, 0
	v_cvt_pk_f16_f32 v124, v180, v181
	v_cvt_pk_f16_f32 v125, v182, v183
	v_pk_max_f16 v124, v124, 0
	v_pk_max_f16 v125, v125, 0
	ds_write_b128 v107, v[122:125]
	v_mfma_f32_16x16x32_f16 v[212:215], v[18:21], v[6:9], 0
	v_mfma_f32_16x16x32_f16 v[228:231], v[10:13], v[6:9], 0
	v_cvt_pk_f16_f32 v126, v168, v169
	v_cvt_pk_f16_f32 v127, v170, v171
	v_pk_max_f16 v126, v126, 0
	v_pk_max_f16 v127, v127, 0
	v_cvt_pk_f16_f32 v128, v184, v185
	v_cvt_pk_f16_f32 v129, v186, v187
	v_pk_max_f16 v128, v128, 0
	v_pk_max_f16 v129, v129, 0
	ds_write_b128 v107, v[126:129] offset:16384
	v_mfma_f32_16x16x32_f16 v[216:219], v[18:21], v[14:17], 0
	v_mfma_f32_16x16x32_f16 v[232:235], v[10:13], v[14:17], 0
	v_cvt_pk_f16_f32 v134, v172, v173
	v_cvt_pk_f16_f32 v135, v174, v175
	v_pk_max_f16 v134, v134, 0
	v_pk_max_f16 v135, v135, 0
	v_cvt_pk_f16_f32 v136, v188, v189
	v_cvt_pk_f16_f32 v137, v190, v191
	v_pk_max_f16 v136, v136, 0
	v_pk_max_f16 v137, v137, 0
	ds_write_b128 v107, v[134:137] offset:32768
	v_mfma_f32_16x16x32_f16 v[220:223], v[18:21], v[26:29], 0
	v_mfma_f32_16x16x32_f16 v[236:239], v[10:13], v[26:29], 0
	v_cvt_pk_f16_f32 v138, v176, v177
	v_cvt_pk_f16_f32 v139, v178, v179
	v_pk_max_f16 v138, v138, 0
	v_pk_max_f16 v139, v139, 0
	v_cvt_pk_f16_f32 v140, v192, v193
	v_cvt_pk_f16_f32 v141, v194, v195
	v_pk_max_f16 v140, v140, 0
	v_pk_max_f16 v141, v141, 0
	ds_write_b128 v107, v[138:141] offset:49152
	v_add_u32_e32 v111, s64, v111
	v_add_u32_e32 v98, s65, v98
	s_lshl_b32 s20, s9, 7
	v_lshl_add_u64 v[0:1], s[20:21], 3, v[132:133]
	s_add_i32 s25, s22, s34
	s_lshl_b32 s8, s9, 8
	buffer_load_dwordx4 v[192:195], v147, s[16:19], s25 offen
	buffer_load_dwordx4 v[196:199], v148, s[16:19], s25 offen
	buffer_load_dwordx4 v[200:203], v149, s[16:19], s25 offen
	buffer_load_dwordx4 v[204:207], v150, s[16:19], s25 offen
	s_waitcnt vmcnt(19) lgkmcnt(4)
	v_mfma_f32_16x16x32_f16 v[164:167], v[58:61], v[122:125], v[240:243]
	s_load_dword s30, s[12:13], 0x0
	v_cvt_pk_f16_f32 v142, v208, v209
	v_cvt_pk_f16_f32 v143, v210, v211
	v_mfma_f32_16x16x32_f16 v[168:171], v[58:61], v[126:129], v[240:243]
	v_pk_max_f16 v142, v142, 0
	v_pk_max_f16 v143, v143, 0
	v_mfma_f32_16x16x32_f16 v[172:175], v[58:61], v[134:137], v[240:243]
	v_cvt_pk_f16_f32 v144, v224, v225
	v_cvt_pk_f16_f32 v145, v226, v227
	v_mfma_f32_16x16x32_f16 v[10:13], v[58:61], v[138:141], v[240:243]
	v_pk_max_f16 v144, v144, 0
	v_pk_max_f16 v145, v145, 0
	ds_write_b128 v108, v[142:145]
	s_waitcnt vmcnt(18)
	v_mfma_f32_16x16x32_f16 v[58:61], v[54:57], v[122:125], v[244:247]
	v_cvt_pk_f16_f32 v152, v212, v213
	v_cvt_pk_f16_f32 v153, v214, v215
	v_mfma_f32_16x16x32_f16 v[176:179], v[54:57], v[126:129], v[244:247]
	v_pk_max_f16 v152, v152, 0
	v_pk_max_f16 v153, v153, 0
	v_mfma_f32_16x16x32_f16 v[180:183], v[54:57], v[134:137], v[244:247]
	v_cvt_pk_f16_f32 v154, v228, v229
	v_cvt_pk_f16_f32 v155, v230, v231
	v_mfma_f32_16x16x32_f16 v[18:21], v[54:57], v[138:141], v[244:247]
	v_pk_max_f16 v154, v154, 0
	v_pk_max_f16 v155, v155, 0
	ds_write_b128 v108, v[152:155] offset:16384
	s_waitcnt vmcnt(17)
	v_mfma_f32_16x16x32_f16 v[54:57], v[50:53], v[122:125], v[248:251]
	v_cvt_pk_f16_f32 v156, v216, v217
	v_cvt_pk_f16_f32 v157, v218, v219
	v_mfma_f32_16x16x32_f16 v[184:187], v[50:53], v[126:129], v[248:251]
	v_pk_max_f16 v156, v156, 0
	v_pk_max_f16 v157, v157, 0
	v_mfma_f32_16x16x32_f16 v[188:191], v[50:53], v[134:137], v[248:251]
	v_cvt_pk_f16_f32 v158, v232, v233
	v_cvt_pk_f16_f32 v159, v234, v235
	v_mfma_f32_16x16x32_f16 v[22:25], v[50:53], v[138:141], v[248:251]
	v_pk_max_f16 v158, v158, 0
	v_pk_max_f16 v159, v159, 0
	ds_write_b128 v108, v[156:159] offset:32768
	s_waitcnt vmcnt(16)
	v_mfma_f32_16x16x32_f16 v[50:53], v[38:41], v[122:125], v[252:255]
	v_cvt_pk_f16_f32 v160, v220, v221
	v_cvt_pk_f16_f32 v161, v222, v223
	v_mfma_f32_16x16x32_f16 v[122:125], v[38:41], v[126:129], v[252:255]
	v_pk_max_f16 v160, v160, 0
	v_pk_max_f16 v161, v161, 0
	v_mfma_f32_16x16x32_f16 v[126:129], v[38:41], v[134:137], v[252:255]
	v_cvt_pk_f16_f32 v162, v236, v237
	v_cvt_pk_f16_f32 v163, v238, v239
	v_mfma_f32_16x16x32_f16 v[38:41], v[38:41], v[138:141], v[252:255]
	v_pk_max_f16 v162, v162, 0
	v_pk_max_f16 v163, v163, 0
	ds_write_b128 v108, v[160:163] offset:49152
	s_add_i32 s9, s22, s35
	s_waitcnt vmcnt(15)
	v_mfma_f32_16x16x32_f16 v[164:167], v[94:97], v[142:145], v[164:167]
	v_mfma_f32_16x16x32_f16 v[168:171], v[94:97], v[152:155], v[168:171]
	s_waitcnt vmcnt(14)
	v_mfma_f32_16x16x32_f16 v[58:61], v[90:93], v[142:145], v[58:61]
	v_mfma_f32_16x16x32_f16 v[176:179], v[90:93], v[152:155], v[176:179]
	s_waitcnt vmcnt(13)
	v_mfma_f32_16x16x32_f16 v[54:57], v[78:81], v[142:145], v[54:57]
	v_mfma_f32_16x16x32_f16 v[184:187], v[78:81], v[152:155], v[184:187]
	s_waitcnt vmcnt(12)
	v_mfma_f32_16x16x32_f16 v[50:53], v[34:37], v[142:145], v[50:53]
	buffer_load_dwordx4 v[140:143], v147, s[16:19], s9 offen
	buffer_load_dwordx4 v[220:223], v148, s[16:19], s9 offen
	v_mfma_f32_16x16x32_f16 v[122:125], v[34:37], v[152:155], v[122:125]
	buffer_load_dwordx4 v[152:155], v149, s[16:19], s9 offen
	buffer_load_dwordx4 v[224:227], v150, s[16:19], s9 offen
	s_mov_b32 s9, s21
	s_waitcnt lgkmcnt(0)
	s_barrier
	v_add_u32_e32 v99, s66, v99
	ds_read_b128 v[136:139], v99
	ds_read_b128 v[208:211], v99 offset:16384
	ds_read_b128 v[212:215], v99 offset:32768
	ds_read_b128 v[216:219], v99 offset:49152
	v_mfma_f32_16x16x32_f16 v[172:175], v[94:97], v[156:159], v[172:175]
	v_mfma_f32_16x16x32_f16 v[94:97], v[94:97], v[160:163], v[10:13]
	s_nop 2
	v_lshl_add_u64 v[10:11], s[8:9], 4, v[130:131]
	v_mfma_f32_16x16x32_f16 v[180:183], v[90:93], v[156:159], v[180:183]
	v_mfma_f32_16x16x32_f16 v[90:93], v[90:93], v[160:163], v[18:21]
	v_mfma_f32_16x16x32_f16 v[188:191], v[78:81], v[156:159], v[188:191]
	v_mfma_f32_16x16x32_f16 v[78:81], v[78:81], v[160:163], v[22:25]
	global_load_dwordx4 v[30:33], v[10:11], off
	s_nop 1
	global_load_dwordx4 v[22:25], v[10:11], off offset:1024
	global_load_dwordx4 v[18:21], v[10:11], off offset:2048
	s_nop 0
	global_load_dwordx4 v[10:13], v[10:11], off offset:3072
	s_nop 0
	global_load_dwordx2 v[134:135], v[0:1], off
	v_mfma_f32_16x16x32_f16 v[126:129], v[34:37], v[156:159], v[126:129]
	v_mfma_f32_16x16x32_f16 v[34:37], v[34:37], v[160:163], v[38:41]
	s_nop 2
	v_add_u32_e32 v100, s67, v100
	ds_read_b128 v[38:41], v100
	ds_read_b128 v[156:159], v100 offset:16384
	ds_read_b128 v[160:163], v100 offset:32768
	ds_read_b128 v[228:231], v100 offset:49152
	s_add_i32 s8, s22, s36
	s_waitcnt vmcnt(20) lgkmcnt(7)
	v_mfma_f32_16x16x32_f16 v[164:167], v[82:85], v[136:139], v[164:167]
	s_waitcnt lgkmcnt(6)
	v_mfma_f32_16x16x32_f16 v[168:171], v[82:85], v[208:211], v[168:171]
	s_waitcnt lgkmcnt(5)
	v_mfma_f32_16x16x32_f16 v[172:175], v[82:85], v[212:215], v[172:175]
	s_waitcnt lgkmcnt(4)
	v_mfma_f32_16x16x32_f16 v[82:85], v[82:85], v[216:219], v[94:97]
	s_waitcnt vmcnt(19)
	v_mfma_f32_16x16x32_f16 v[58:61], v[70:73], v[136:139], v[58:61]
	v_mfma_f32_16x16x32_f16 v[94:97], v[70:73], v[208:211], v[176:179]
	v_mfma_f32_16x16x32_f16 v[176:179], v[70:73], v[212:215], v[180:183]
	v_mfma_f32_16x16x32_f16 v[70:73], v[70:73], v[216:219], v[90:93]
	s_waitcnt vmcnt(18)
	v_mfma_f32_16x16x32_f16 v[54:57], v[62:65], v[136:139], v[54:57]
	v_mfma_f32_16x16x32_f16 v[90:93], v[62:65], v[208:211], v[184:187]
	v_mfma_f32_16x16x32_f16 v[180:183], v[62:65], v[212:215], v[188:191]
	v_mfma_f32_16x16x32_f16 v[62:65], v[62:65], v[216:219], v[78:81]
	s_waitcnt vmcnt(17)
	v_mfma_f32_16x16x32_f16 v[50:53], v[42:45], v[136:139], v[50:53]
	v_mfma_f32_16x16x32_f16 v[78:81], v[42:45], v[208:211], v[122:125]
	v_mfma_f32_16x16x32_f16 v[122:125], v[42:45], v[212:215], v[126:129]
	s_nop 2
	buffer_load_dwordx4 v[126:129], v147, s[16:19], s8 offen
	buffer_load_dwordx4 v[136:139], v148, s[16:19], s8 offen
	buffer_load_dwordx4 v[184:187], v149, s[16:19], s8 offen
	buffer_load_dwordx4 v[188:191], v150, s[16:19], s8 offen
	v_mfma_f32_16x16x32_f16 v[34:37], v[42:45], v[216:219], v[34:37]
	v_add_u32_e32 v111, s68, v111
	ds_read_b128 v[42:45], v111
	ds_read_b128 v[208:211], v111 offset:16384
	ds_read_b128 v[212:215], v111 offset:32768
	ds_read_b128 v[216:219], v111 offset:49152
	s_add_i32 s8, s22, s37
	s_waitcnt vmcnt(20) lgkmcnt(7)
	v_mfma_f32_16x16x32_f16 v[164:167], v[86:89], v[38:41], v[164:167]
	s_waitcnt lgkmcnt(6)
	v_mfma_f32_16x16x32_f16 v[168:171], v[86:89], v[156:159], v[168:171]
	s_waitcnt lgkmcnt(5)
	v_mfma_f32_16x16x32_f16 v[172:175], v[86:89], v[160:163], v[172:175]
	s_waitcnt lgkmcnt(4)
	v_mfma_f32_16x16x32_f16 v[82:85], v[86:89], v[228:231], v[82:85]
	s_waitcnt vmcnt(19)
	v_mfma_f32_16x16x32_f16 v[58:61], v[74:77], v[38:41], v[58:61]
	v_mfma_f32_16x16x32_f16 v[86:89], v[74:77], v[156:159], v[94:97]
	v_mfma_f32_16x16x32_f16 v[94:97], v[74:77], v[160:163], v[176:179]
	v_mfma_f32_16x16x32_f16 v[70:73], v[74:77], v[228:231], v[70:73]
	s_waitcnt vmcnt(18)
	v_mfma_f32_16x16x32_f16 v[54:57], v[66:69], v[38:41], v[54:57]
	v_mfma_f32_16x16x32_f16 v[74:77], v[66:69], v[156:159], v[90:93]
	v_mfma_f32_16x16x32_f16 v[90:93], v[66:69], v[160:163], v[180:183]
	v_mfma_f32_16x16x32_f16 v[62:65], v[66:69], v[228:231], v[62:65]
	s_waitcnt vmcnt(17)
	v_mfma_f32_16x16x32_f16 v[38:41], v[46:49], v[38:41], v[50:53]
	v_mfma_f32_16x16x32_f16 v[50:53], v[46:49], v[156:159], v[78:81]
	v_mfma_f32_16x16x32_f16 v[66:69], v[46:49], v[160:163], v[122:125]
	s_nop 1
	buffer_load_dwordx4 v[78:81], v147, s[16:19], s8 offen
	buffer_load_dwordx4 v[122:125], v148, s[16:19], s8 offen
	buffer_load_dwordx4 v[156:159], v149, s[16:19], s8 offen
	buffer_load_dwordx4 v[160:163], v150, s[16:19], s8 offen
	v_mfma_f32_16x16x32_f16 v[34:37], v[46:49], v[228:231], v[34:37]
	v_add_u32_e32 v98, s69, v98
	ds_read_b128 v[46:49], v98
	ds_read_b128 v[176:179], v98 offset:16384
	ds_read_b128 v[180:183], v98 offset:32768
	ds_read_b128 v[228:231], v98 offset:49152
	s_add_i32 s8, s22, s38
	s_waitcnt vmcnt(20) lgkmcnt(7)
	v_mfma_f32_16x16x32_f16 v[164:167], v[192:195], v[42:45], v[164:167]
	s_waitcnt lgkmcnt(6)
	v_mfma_f32_16x16x32_f16 v[168:171], v[192:195], v[208:211], v[168:171]
	s_waitcnt lgkmcnt(5)
	v_mfma_f32_16x16x32_f16 v[172:175], v[192:195], v[212:215], v[172:175]
	s_waitcnt lgkmcnt(4)
	v_mfma_f32_16x16x32_f16 v[82:85], v[192:195], v[216:219], v[82:85]
	s_waitcnt vmcnt(19)
	v_mfma_f32_16x16x32_f16 v[58:61], v[196:199], v[42:45], v[58:61]
	v_mfma_f32_16x16x32_f16 v[86:89], v[196:199], v[208:211], v[86:89]
	v_mfma_f32_16x16x32_f16 v[94:97], v[196:199], v[212:215], v[94:97]
	v_mfma_f32_16x16x32_f16 v[70:73], v[196:199], v[216:219], v[70:73]
	s_waitcnt vmcnt(18)
	v_mfma_f32_16x16x32_f16 v[54:57], v[200:203], v[42:45], v[54:57]
	v_mfma_f32_16x16x32_f16 v[74:77], v[200:203], v[208:211], v[74:77]
	v_mfma_f32_16x16x32_f16 v[90:93], v[200:203], v[212:215], v[90:93]
	v_mfma_f32_16x16x32_f16 v[62:65], v[200:203], v[216:219], v[62:65]
	s_waitcnt vmcnt(17)
	v_mfma_f32_16x16x32_f16 v[38:41], v[204:207], v[42:45], v[38:41]
	v_mfma_f32_16x16x32_f16 v[42:45], v[204:207], v[208:211], v[50:53]
	v_mfma_f32_16x16x32_f16 v[50:53], v[204:207], v[212:215], v[66:69]
	s_nop 2
	buffer_load_dwordx4 v[66:69], v147, s[16:19], s8 offen
	buffer_load_dwordx4 v[192:195], v148, s[16:19], s8 offen
	buffer_load_dwordx4 v[196:199], v149, s[16:19], s8 offen
	buffer_load_dwordx4 v[200:203], v150, s[16:19], s8 offen
	v_mfma_f32_16x16x32_f16 v[34:37], v[204:207], v[216:219], v[34:37]
	v_add_u32_e32 v99, s70, v99
	ds_read_b128 v[204:207], v99
	ds_read_b128 v[208:211], v99 offset:16384
	ds_read_b128 v[212:215], v99 offset:32768
	ds_read_b128 v[216:219], v99 offset:49152
	s_add_i32 s8, s22, s39
	s_waitcnt vmcnt(20) lgkmcnt(7)
	v_mfma_f32_16x16x32_f16 v[164:167], v[140:143], v[46:49], v[164:167]
	s_waitcnt lgkmcnt(6)
	v_mfma_f32_16x16x32_f16 v[168:171], v[140:143], v[176:179], v[168:171]
	s_waitcnt lgkmcnt(5)
	v_mfma_f32_16x16x32_f16 v[172:175], v[140:143], v[180:183], v[172:175]
	s_waitcnt lgkmcnt(4)
	v_mfma_f32_16x16x32_f16 v[82:85], v[140:143], v[228:231], v[82:85]
	s_waitcnt vmcnt(19)
	v_mfma_f32_16x16x32_f16 v[58:61], v[220:223], v[46:49], v[58:61]
	v_mfma_f32_16x16x32_f16 v[86:89], v[220:223], v[176:179], v[86:89]
	s_waitcnt vmcnt(18)
	v_mfma_f32_16x16x32_f16 v[54:57], v[152:155], v[46:49], v[54:57]
	v_mfma_f32_16x16x32_f16 v[74:77], v[152:155], v[176:179], v[74:77]
	v_mfma_f32_16x16x32_f16 v[90:93], v[152:155], v[180:183], v[90:93]
	v_mfma_f32_16x16x32_f16 v[62:65], v[152:155], v[228:231], v[62:65]
	s_waitcnt vmcnt(17)
	v_mfma_f32_16x16x32_f16 v[38:41], v[224:227], v[46:49], v[38:41]
	v_mfma_f32_16x16x32_f16 v[42:45], v[224:227], v[176:179], v[42:45]
	v_mfma_f32_16x16x32_f16 v[46:49], v[224:227], v[180:183], v[50:53]
	s_nop 2
	buffer_load_dwordx4 v[50:53], v147, s[16:19], s8 offen
	buffer_load_dwordx4 v[140:143], v148, s[16:19], s8 offen
	buffer_load_dwordx4 v[152:155], v149, s[16:19], s8 offen
	buffer_load_dwordx4 v[176:179], v150, s[16:19], s8 offen
	v_mfma_f32_16x16x32_f16 v[94:97], v[220:223], v[180:183], v[94:97]
	v_mfma_f32_16x16x32_f16 v[70:73], v[220:223], v[228:231], v[70:73]
	v_mfma_f32_16x16x32_f16 v[34:37], v[224:227], v[228:231], v[34:37]
	v_add_u32_e32 v100, s71, v100
	ds_read_b128 v[180:183], v100
	ds_read_b128 v[220:223], v100 offset:16384
	ds_read_b128 v[224:227], v100 offset:32768
	ds_read_b128 v[228:231], v100 offset:49152
	s_add_i32 s8, s22, s40
	s_waitcnt vmcnt(15) lgkmcnt(7)
	v_mfma_f32_16x16x32_f16 v[164:167], v[126:129], v[204:207], v[164:167]
	s_waitcnt lgkmcnt(6)
	v_mfma_f32_16x16x32_f16 v[168:171], v[126:129], v[208:211], v[168:171]
	s_waitcnt lgkmcnt(5)
	v_mfma_f32_16x16x32_f16 v[172:175], v[126:129], v[212:215], v[172:175]
	s_waitcnt lgkmcnt(4)
	v_mfma_f32_16x16x32_f16 v[82:85], v[126:129], v[216:219], v[82:85]
	s_waitcnt vmcnt(14)
	v_mfma_f32_16x16x32_f16 v[58:61], v[136:139], v[204:207], v[58:61]
	v_mfma_f32_16x16x32_f16 v[86:89], v[136:139], v[208:211], v[86:89]
	v_mfma_f32_16x16x32_f16 v[94:97], v[136:139], v[212:215], v[94:97]
	v_mfma_f32_16x16x32_f16 v[70:73], v[136:139], v[216:219], v[70:73]
	s_waitcnt vmcnt(13)
	v_mfma_f32_16x16x32_f16 v[54:57], v[184:187], v[204:207], v[54:57]
	v_mfma_f32_16x16x32_f16 v[74:77], v[184:187], v[208:211], v[74:77]
	v_mfma_f32_16x16x32_f16 v[90:93], v[184:187], v[212:215], v[90:93]
	v_mfma_f32_16x16x32_f16 v[62:65], v[184:187], v[216:219], v[62:65]
	s_waitcnt vmcnt(12)
	v_mfma_f32_16x16x32_f16 v[38:41], v[188:191], v[204:207], v[38:41]
	buffer_load_dwordx4 v[126:129], v147, s[16:19], s8 offen
	buffer_load_dwordx4 v[136:139], v148, s[16:19], s8 offen
	buffer_load_dwordx4 v[184:187], v149, s[16:19], s8 offen
	buffer_load_dwordx4 v[204:207], v150, s[16:19], s8 offen
	v_mfma_f32_16x16x32_f16 v[42:45], v[188:191], v[208:211], v[42:45]
	v_mfma_f32_16x16x32_f16 v[46:49], v[188:191], v[212:215], v[46:49]
	v_mfma_f32_16x16x32_f16 v[34:37], v[188:191], v[216:219], v[34:37]
	v_add_u32_e32 v111, s72, v111
	ds_read_b128 v[188:191], v111
	ds_read_b128 v[208:211], v111 offset:16384
	ds_read_b128 v[212:215], v111 offset:32768
	ds_read_b128 v[216:219], v111 offset:49152
	s_add_i32 s8, s22, s41
	s_waitcnt vmcnt(15) lgkmcnt(7)
	v_mfma_f32_16x16x32_f16 v[164:167], v[78:81], v[180:183], v[164:167]
	s_waitcnt lgkmcnt(6)
	v_mfma_f32_16x16x32_f16 v[168:171], v[78:81], v[220:223], v[168:171]
	s_waitcnt lgkmcnt(5)
	v_mfma_f32_16x16x32_f16 v[172:175], v[78:81], v[224:227], v[172:175]
	s_waitcnt lgkmcnt(4)
	v_mfma_f32_16x16x32_f16 v[78:81], v[78:81], v[228:231], v[82:85]
	s_waitcnt vmcnt(14)
	v_mfma_f32_16x16x32_f16 v[58:61], v[122:125], v[180:183], v[58:61]
	v_mfma_f32_16x16x32_f16 v[82:85], v[122:125], v[220:223], v[86:89]
	v_mfma_f32_16x16x32_f16 v[86:89], v[122:125], v[224:227], v[94:97]
	v_mfma_f32_16x16x32_f16 v[70:73], v[122:125], v[228:231], v[70:73]
	s_waitcnt vmcnt(13)
	v_mfma_f32_16x16x32_f16 v[54:57], v[156:159], v[180:183], v[54:57]
	v_mfma_f32_16x16x32_f16 v[74:77], v[156:159], v[220:223], v[74:77]
	v_mfma_f32_16x16x32_f16 v[90:93], v[156:159], v[224:227], v[90:93]
	v_mfma_f32_16x16x32_f16 v[62:65], v[156:159], v[228:231], v[62:65]
	s_waitcnt vmcnt(12)
	v_mfma_f32_16x16x32_f16 v[38:41], v[160:163], v[180:183], v[38:41]
	buffer_load_dwordx4 v[94:97], v147, s[16:19], s8 offen
	buffer_load_dwordx4 v[122:125], v148, s[16:19], s8 offen
	buffer_load_dwordx4 v[156:159], v149, s[16:19], s8 offen
	buffer_load_dwordx4 v[180:183], v150, s[16:19], s8 offen
	v_mfma_f32_16x16x32_f16 v[42:45], v[160:163], v[220:223], v[42:45]
	v_mfma_f32_16x16x32_f16 v[46:49], v[160:163], v[224:227], v[46:49]
	v_mfma_f32_16x16x32_f16 v[34:37], v[160:163], v[228:231], v[34:37]
	v_add_u32_e32 v98, s73, v98
	ds_read_b128 v[160:163], v98
	ds_read_b128 v[220:223], v98 offset:16384
	ds_read_b128 v[224:227], v98 offset:32768
	ds_read_b128 v[228:231], v98 offset:49152
	s_add_i32 s8, s22, s42
	s_waitcnt vmcnt(15) lgkmcnt(7)
	v_mfma_f32_16x16x32_f16 v[164:167], v[66:69], v[188:191], v[164:167]
	s_waitcnt lgkmcnt(6)
	v_mfma_f32_16x16x32_f16 v[168:171], v[66:69], v[208:211], v[168:171]
	s_waitcnt lgkmcnt(5)
	v_mfma_f32_16x16x32_f16 v[172:175], v[66:69], v[212:215], v[172:175]
	s_waitcnt lgkmcnt(4)
	v_mfma_f32_16x16x32_f16 v[66:69], v[66:69], v[216:219], v[78:81]
	s_waitcnt vmcnt(14)
	v_mfma_f32_16x16x32_f16 v[58:61], v[192:195], v[188:191], v[58:61]
	v_mfma_f32_16x16x32_f16 v[78:81], v[192:195], v[208:211], v[82:85]
	v_mfma_f32_16x16x32_f16 v[82:85], v[192:195], v[212:215], v[86:89]
	v_mfma_f32_16x16x32_f16 v[70:73], v[192:195], v[216:219], v[70:73]
	s_waitcnt vmcnt(13)
	v_mfma_f32_16x16x32_f16 v[54:57], v[196:199], v[188:191], v[54:57]
	v_mfma_f32_16x16x32_f16 v[74:77], v[196:199], v[208:211], v[74:77]
	v_mfma_f32_16x16x32_f16 v[86:89], v[196:199], v[212:215], v[90:93]
	v_mfma_f32_16x16x32_f16 v[62:65], v[196:199], v[216:219], v[62:65]
	s_waitcnt vmcnt(12)
	v_mfma_f32_16x16x32_f16 v[38:41], v[200:203], v[188:191], v[38:41]
	buffer_load_dwordx4 v[90:93], v147, s[16:19], s8 offen
	buffer_load_dwordx4 v[188:191], v148, s[16:19], s8 offen
	buffer_load_dwordx4 v[192:195], v149, s[16:19], s8 offen
	buffer_load_dwordx4 v[196:199], v150, s[16:19], s8 offen
	v_mfma_f32_16x16x32_f16 v[42:45], v[200:203], v[208:211], v[42:45]
	v_mfma_f32_16x16x32_f16 v[46:49], v[200:203], v[212:215], v[46:49]
	v_mfma_f32_16x16x32_f16 v[34:37], v[200:203], v[216:219], v[34:37]
	v_add_u32_e32 v99, s74, v99
	ds_read_b128 v[200:203], v99
	ds_read_b128 v[208:211], v99 offset:16384
	ds_read_b128 v[212:215], v99 offset:32768
	ds_read_b128 v[216:219], v99 offset:49152
	s_add_i32 s8, s22, s43
	s_waitcnt vmcnt(15) lgkmcnt(7)
	v_mfma_f32_16x16x32_f16 v[164:167], v[50:53], v[160:163], v[164:167]
	s_waitcnt lgkmcnt(6)
	v_mfma_f32_16x16x32_f16 v[168:171], v[50:53], v[220:223], v[168:171]
	s_waitcnt lgkmcnt(5)
	v_mfma_f32_16x16x32_f16 v[172:175], v[50:53], v[224:227], v[172:175]
	s_waitcnt lgkmcnt(4)
	v_mfma_f32_16x16x32_f16 v[50:53], v[50:53], v[228:231], v[66:69]
	s_waitcnt vmcnt(14)
	v_mfma_f32_16x16x32_f16 v[58:61], v[140:143], v[160:163], v[58:61]
	v_mfma_f32_16x16x32_f16 v[66:69], v[140:143], v[220:223], v[78:81]
	v_mfma_f32_16x16x32_f16 v[78:81], v[140:143], v[224:227], v[82:85]
	v_mfma_f32_16x16x32_f16 v[70:73], v[140:143], v[228:231], v[70:73]
	s_waitcnt vmcnt(13)
	v_mfma_f32_16x16x32_f16 v[54:57], v[152:155], v[160:163], v[54:57]
	v_mfma_f32_16x16x32_f16 v[74:77], v[152:155], v[220:223], v[74:77]
	v_mfma_f32_16x16x32_f16 v[82:85], v[152:155], v[224:227], v[86:89]
	v_mfma_f32_16x16x32_f16 v[62:65], v[152:155], v[228:231], v[62:65]
	s_waitcnt vmcnt(12)
	v_mfma_f32_16x16x32_f16 v[38:41], v[176:179], v[160:163], v[38:41]
	buffer_load_dwordx4 v[86:89], v147, s[16:19], s8 offen
	buffer_load_dwordx4 v[140:143], v148, s[16:19], s8 offen
	buffer_load_dwordx4 v[152:155], v149, s[16:19], s8 offen
	buffer_load_dwordx4 v[160:163], v150, s[16:19], s8 offen
	v_mfma_f32_16x16x32_f16 v[42:45], v[176:179], v[220:223], v[42:45]
	v_mfma_f32_16x16x32_f16 v[46:49], v[176:179], v[224:227], v[46:49]
	v_mfma_f32_16x16x32_f16 v[34:37], v[176:179], v[228:231], v[34:37]
	v_add_u32_e32 v100, s75, v100
	ds_read_b128 v[176:179], v100
	ds_read_b128 v[220:223], v100 offset:16384
	ds_read_b128 v[224:227], v100 offset:32768
	ds_read_b128 v[228:231], v100 offset:49152
	s_add_i32 s8, s22, s44
	s_waitcnt vmcnt(15) lgkmcnt(7)
	v_mfma_f32_16x16x32_f16 v[164:167], v[126:129], v[200:203], v[164:167]
	s_waitcnt lgkmcnt(6)
	v_mfma_f32_16x16x32_f16 v[168:171], v[126:129], v[208:211], v[168:171]
	s_waitcnt lgkmcnt(5)
	v_mfma_f32_16x16x32_f16 v[172:175], v[126:129], v[212:215], v[172:175]
	s_waitcnt lgkmcnt(4)
	v_mfma_f32_16x16x32_f16 v[50:53], v[126:129], v[216:219], v[50:53]
	s_waitcnt vmcnt(14)
	v_mfma_f32_16x16x32_f16 v[58:61], v[136:139], v[200:203], v[58:61]
	v_mfma_f32_16x16x32_f16 v[66:69], v[136:139], v[208:211], v[66:69]
	v_mfma_f32_16x16x32_f16 v[78:81], v[136:139], v[212:215], v[78:81]
	v_mfma_f32_16x16x32_f16 v[70:73], v[136:139], v[216:219], v[70:73]
	s_waitcnt vmcnt(13)
	v_mfma_f32_16x16x32_f16 v[54:57], v[184:187], v[200:203], v[54:57]
	v_mfma_f32_16x16x32_f16 v[74:77], v[184:187], v[208:211], v[74:77]
	v_mfma_f32_16x16x32_f16 v[82:85], v[184:187], v[212:215], v[82:85]
	v_mfma_f32_16x16x32_f16 v[62:65], v[184:187], v[216:219], v[62:65]
	s_waitcnt vmcnt(12)
	v_mfma_f32_16x16x32_f16 v[38:41], v[204:207], v[200:203], v[38:41]
	buffer_load_dwordx4 v[126:129], v147, s[16:19], s8 offen
	buffer_load_dwordx4 v[136:139], v148, s[16:19], s8 offen
	buffer_load_dwordx4 v[184:187], v149, s[16:19], s8 offen
	buffer_load_dwordx4 v[200:203], v150, s[16:19], s8 offen
	v_mfma_f32_16x16x32_f16 v[42:45], v[204:207], v[208:211], v[42:45]
	v_mfma_f32_16x16x32_f16 v[46:49], v[204:207], v[212:215], v[46:49]
	v_mfma_f32_16x16x32_f16 v[34:37], v[204:207], v[216:219], v[34:37]
	v_add_u32_e32 v111, s76, v111
	ds_read_b128 v[204:207], v111
	ds_read_b128 v[208:211], v111 offset:16384
	ds_read_b128 v[212:215], v111 offset:32768
	ds_read_b128 v[216:219], v111 offset:49152
	s_add_i32 s8, s22, s45
	s_waitcnt vmcnt(15) lgkmcnt(7)
	v_mfma_f32_16x16x32_f16 v[164:167], v[94:97], v[176:179], v[164:167]
	s_waitcnt lgkmcnt(6)
	v_mfma_f32_16x16x32_f16 v[168:171], v[94:97], v[220:223], v[168:171]
	s_waitcnt vmcnt(14)
	v_mfma_f32_16x16x32_f16 v[58:61], v[122:125], v[176:179], v[58:61]
	v_mfma_f32_16x16x32_f16 v[66:69], v[122:125], v[220:223], v[66:69]
	s_waitcnt lgkmcnt(5)
	v_mfma_f32_16x16x32_f16 v[78:81], v[122:125], v[224:227], v[78:81]
	s_waitcnt lgkmcnt(4)
	v_mfma_f32_16x16x32_f16 v[70:73], v[122:125], v[228:231], v[70:73]
	s_waitcnt vmcnt(13)
	v_mfma_f32_16x16x32_f16 v[54:57], v[156:159], v[176:179], v[54:57]
	v_mfma_f32_16x16x32_f16 v[74:77], v[156:159], v[220:223], v[74:77]
	v_mfma_f32_16x16x32_f16 v[82:85], v[156:159], v[224:227], v[82:85]
	v_mfma_f32_16x16x32_f16 v[62:65], v[156:159], v[228:231], v[62:65]
	s_waitcnt vmcnt(12)
	v_mfma_f32_16x16x32_f16 v[38:41], v[180:183], v[176:179], v[38:41]
	v_mfma_f32_16x16x32_f16 v[42:45], v[180:183], v[220:223], v[42:45]
	buffer_load_dwordx4 v[122:125], v147, s[16:19], s8 offen
	buffer_load_dwordx4 v[156:159], v148, s[16:19], s8 offen
	buffer_load_dwordx4 v[176:179], v149, s[16:19], s8 offen
	buffer_load_dwordx4 v[220:223], v150, s[16:19], s8 offen
	v_mfma_f32_16x16x32_f16 v[50:53], v[94:97], v[228:231], v[50:53]
	v_mfma_f32_16x16x32_f16 v[46:49], v[180:183], v[224:227], v[46:49]
	v_mfma_f32_16x16x32_f16 v[34:37], v[180:183], v[228:231], v[34:37]
	v_mfma_f32_16x16x32_f16 v[172:175], v[94:97], v[224:227], v[172:175]
	v_add_u32_e32 v98, s77, v98
	ds_read_b128 v[94:97], v98
	ds_read_b128 v[180:183], v98 offset:16384
	ds_read_b128 v[224:227], v98 offset:32768
	ds_read_b128 v[228:231], v98 offset:49152
	s_add_i32 s8, s22, s46
	s_waitcnt vmcnt(15) lgkmcnt(7)
	v_mfma_f32_16x16x32_f16 v[164:167], v[90:93], v[204:207], v[164:167]
	s_waitcnt lgkmcnt(6)
	v_mfma_f32_16x16x32_f16 v[168:171], v[90:93], v[208:211], v[168:171]
	s_waitcnt lgkmcnt(5)
	v_mfma_f32_16x16x32_f16 v[172:175], v[90:93], v[212:215], v[172:175]
	s_waitcnt lgkmcnt(4)
	v_mfma_f32_16x16x32_f16 v[90:93], v[90:93], v[216:219], v[50:53]
	s_waitcnt vmcnt(14)
	v_mfma_f32_16x16x32_f16 v[232:235], v[188:191], v[204:207], v[58:61]
	v_mfma_f32_16x16x32_f16 v[66:69], v[188:191], v[208:211], v[66:69]
	v_mfma_f32_16x16x32_f16 v[78:81], v[188:191], v[212:215], v[78:81]
	v_mfma_f32_16x16x32_f16 v[70:73], v[188:191], v[216:219], v[70:73]
	s_waitcnt vmcnt(13)
	v_mfma_f32_16x16x32_f16 v[188:191], v[192:195], v[204:207], v[54:57]
	v_mfma_f32_16x16x32_f16 v[74:77], v[192:195], v[208:211], v[74:77]
	v_mfma_f32_16x16x32_f16 v[82:85], v[192:195], v[212:215], v[82:85]
	v_mfma_f32_16x16x32_f16 v[62:65], v[192:195], v[216:219], v[62:65]
	s_waitcnt vmcnt(12)
	v_mfma_f32_16x16x32_f16 v[192:195], v[196:199], v[204:207], v[38:41]
	buffer_load_dwordx4 v[58:61], v147, s[16:19], s8 offen
	buffer_load_dwordx4 v[54:57], v148, s[16:19], s8 offen
	buffer_load_dwordx4 v[50:53], v149, s[16:19], s8 offen
	buffer_load_dwordx4 v[38:41], v150, s[16:19], s8 offen
	v_mfma_f32_16x16x32_f16 v[42:45], v[196:199], v[208:211], v[42:45]
	v_mfma_f32_16x16x32_f16 v[46:49], v[196:199], v[212:215], v[46:49]
	v_mfma_f32_16x16x32_f16 v[196:199], v[196:199], v[216:219], v[34:37]
	v_add_u32_e32 v99, s78, v99
	ds_read_b128 v[204:207], v99
	ds_read_b128 v[208:211], v99 offset:16384
	ds_read_b128 v[212:215], v99 offset:32768
	ds_read_b128 v[216:219], v99 offset:49152
	s_add_i32 s8, s22, s47
	s_waitcnt vmcnt(15) lgkmcnt(7)
	v_mfma_f32_16x16x32_f16 v[164:167], v[86:89], v[94:97], v[164:167]
	s_waitcnt lgkmcnt(6)
	v_mfma_f32_16x16x32_f16 v[168:171], v[86:89], v[180:183], v[168:171]
	s_waitcnt lgkmcnt(5)
	v_mfma_f32_16x16x32_f16 v[172:175], v[86:89], v[224:227], v[172:175]
	s_waitcnt lgkmcnt(4)
	v_mfma_f32_16x16x32_f16 v[86:89], v[86:89], v[228:231], v[90:93]
	s_waitcnt vmcnt(14)
	v_mfma_f32_16x16x32_f16 v[232:235], v[140:143], v[94:97], v[232:235]
	v_mfma_f32_16x16x32_f16 v[66:69], v[140:143], v[180:183], v[66:69]
	v_mfma_f32_16x16x32_f16 v[236:239], v[140:143], v[224:227], v[78:81]
	v_mfma_f32_16x16x32_f16 v[70:73], v[140:143], v[228:231], v[70:73]
	s_waitcnt vmcnt(13)
	v_mfma_f32_16x16x32_f16 v[140:143], v[152:155], v[94:97], v[188:191]
	v_mfma_f32_16x16x32_f16 v[74:77], v[152:155], v[180:183], v[74:77]
	v_mfma_f32_16x16x32_f16 v[82:85], v[152:155], v[224:227], v[82:85]
	v_mfma_f32_16x16x32_f16 v[62:65], v[152:155], v[228:231], v[62:65]
	s_waitcnt vmcnt(12)
	v_mfma_f32_16x16x32_f16 v[152:155], v[160:163], v[94:97], v[192:195]
	buffer_load_dwordx4 v[94:97], v147, s[16:19], s8 offen
	buffer_load_dwordx4 v[90:93], v148, s[16:19], s8 offen
	buffer_load_dwordx4 v[78:81], v149, s[16:19], s8 offen
	buffer_load_dwordx4 v[34:37], v150, s[16:19], s8 offen
	v_mfma_f32_16x16x32_f16 v[42:45], v[160:163], v[180:183], v[42:45]
	v_mfma_f32_16x16x32_f16 v[46:49], v[160:163], v[224:227], v[46:49]
	v_mfma_f32_16x16x32_f16 v[160:163], v[160:163], v[228:231], v[196:199]
	v_add_u32_e32 v100, s79, v100
	ds_read_b128 v[180:183], v100
	ds_read_b128 v[188:191], v100 offset:16384
	ds_read_b128 v[192:195], v100 offset:32768
	ds_read_b128 v[196:199], v100 offset:49152
	s_add_i32 s8, s22, s48
	s_waitcnt vmcnt(15) lgkmcnt(7)
	v_mfma_f32_16x16x32_f16 v[164:167], v[126:129], v[204:207], v[164:167]
	s_waitcnt lgkmcnt(6)
	v_mfma_f32_16x16x32_f16 v[168:171], v[126:129], v[208:211], v[168:171]
	s_waitcnt lgkmcnt(5)
	v_mfma_f32_16x16x32_f16 v[172:175], v[126:129], v[212:215], v[172:175]
	s_waitcnt lgkmcnt(4)
	v_mfma_f32_16x16x32_f16 v[86:89], v[126:129], v[216:219], v[86:89]
	s_waitcnt vmcnt(14)
	v_mfma_f32_16x16x32_f16 v[126:129], v[136:139], v[204:207], v[232:235]
	v_mfma_f32_16x16x32_f16 v[66:69], v[136:139], v[208:211], v[66:69]
	v_mfma_f32_16x16x32_f16 v[224:227], v[136:139], v[212:215], v[236:239]
	v_mfma_f32_16x16x32_f16 v[136:139], v[136:139], v[216:219], v[70:73]
	s_waitcnt vmcnt(13)
	v_mfma_f32_16x16x32_f16 v[140:143], v[184:187], v[204:207], v[140:143]
	v_mfma_f32_16x16x32_f16 v[74:77], v[184:187], v[208:211], v[74:77]
	v_mfma_f32_16x16x32_f16 v[228:231], v[184:187], v[212:215], v[82:85]
	v_mfma_f32_16x16x32_f16 v[184:187], v[184:187], v[216:219], v[62:65]
	s_waitcnt vmcnt(12)
	v_mfma_f32_16x16x32_f16 v[152:155], v[200:203], v[204:207], v[152:155]
	v_mfma_f32_16x16x32_f16 v[204:207], v[200:203], v[208:211], v[42:45]
	buffer_load_dwordx4 v[82:85], v147, s[16:19], s8 offen
	buffer_load_dwordx4 v[70:73], v148, s[16:19], s8 offen
	buffer_load_dwordx4 v[62:65], v149, s[16:19], s8 offen
	buffer_load_dwordx4 v[42:45], v150, s[16:19], s8 offen
	v_mfma_f32_16x16x32_f16 v[46:49], v[200:203], v[212:215], v[46:49]
	v_mfma_f32_16x16x32_f16 v[160:163], v[200:203], v[216:219], v[160:163]
	v_add_u32_e32 v0, 0x1ac00, v104
	ds_read_b128 v[240:243], v0
	ds_read_b128 v[244:247], v0 offset:16
	s_waitcnt vmcnt(12) lgkmcnt(5)
	v_mfma_f32_16x16x32_f16 v[164:167], v[122:125], v[180:183], v[164:167]
	v_mfma_f32_16x16x32_f16 v[126:129], v[156:159], v[180:183], v[126:129]
	v_mfma_f32_16x16x32_f16 v[140:143], v[176:179], v[180:183], v[140:143]
	v_mfma_f32_16x16x32_f16 v[152:155], v[220:223], v[180:183], v[152:155]
	s_waitcnt lgkmcnt(4)
	v_mfma_f32_16x16x32_f16 v[168:171], v[122:125], v[188:191], v[168:171]
	v_mfma_f32_16x16x32_f16 v[208:211], v[156:159], v[188:191], v[66:69]
	v_mfma_f32_16x16x32_f16 v[212:215], v[176:179], v[188:191], v[74:77]
	v_mfma_f32_16x16x32_f16 v[204:207], v[220:223], v[188:191], v[204:207]
	s_waitcnt lgkmcnt(3)
	v_mfma_f32_16x16x32_f16 v[172:175], v[122:125], v[192:195], v[172:175]
	v_cvt_pk_f16_f32 v232, v164, v165
	v_cvt_pk_f16_f32 v233, v166, v167
	v_pk_max_f16 v232, v232, 0
	v_pk_max_f16 v233, v233, 0
	v_mfma_f32_16x16x32_f16 v[224:227], v[156:159], v[192:195], v[224:227]
	v_cvt_pk_f16_f32 v234, v126, v127
	v_cvt_pk_f16_f32 v235, v128, v129
	v_pk_max_f16 v234, v234, 0
	v_pk_max_f16 v235, v235, 0
	v_mfma_f32_16x16x32_f16 v[228:231], v[176:179], v[192:195], v[228:231]
	v_cvt_pk_f16_f32 v236, v140, v141
	v_cvt_pk_f16_f32 v237, v142, v143
	v_pk_max_f16 v236, v236, 0
	v_pk_max_f16 v237, v237, 0
	v_mfma_f32_16x16x32_f16 v[216:219], v[220:223], v[192:195], v[46:49]
	v_cvt_pk_f16_f32 v238, v152, v153
	v_cvt_pk_f16_f32 v239, v154, v155
	v_pk_max_f16 v238, v238, 0
	v_pk_max_f16 v239, v239, 0
	s_waitcnt lgkmcnt(2)
	v_mfma_f32_16x16x32_f16 v[200:203], v[122:125], v[196:199], v[86:89]
	v_cvt_pk_f16_f32 v180, v168, v169
	v_cvt_pk_f16_f32 v181, v170, v171
	v_pk_max_f16 v180, v180, 0
	v_pk_max_f16 v181, v181, 0
	s_add_i32 s8, s22, s49
	buffer_load_dwordx4 v[86:89], v147, s[16:19], s8 offen
	buffer_load_dwordx4 v[74:77], v148, s[16:19], s8 offen
	buffer_load_dwordx4 v[66:69], v149, s[16:19], s8 offen
	buffer_load_dwordx4 v[46:49], v150, s[16:19], s8 offen
	v_mfma_f32_16x16x32_f16 v[136:139], v[156:159], v[196:199], v[136:139]
	v_cvt_pk_f16_f32 v182, v208, v209
	v_cvt_pk_f16_f32 v183, v210, v211
	v_pk_max_f16 v182, v182, 0
	v_pk_max_f16 v183, v183, 0
	s_waitcnt lgkmcnt(1)
	v_mfma_f32_16x16x32_f16 v[252:255], v[240:243], v[232:235], 0
	v_cvt_pk_f16_f32 v232, v172, v173
	v_cvt_pk_f16_f32 v233, v174, v175
	v_pk_max_f16 v232, v232, 0
	v_pk_max_f16 v233, v233, 0
	v_mfma_f32_16x16x32_f16 v[184:187], v[176:179], v[196:199], v[184:187]
	v_cvt_pk_f16_f32 v188, v212, v213
	v_cvt_pk_f16_f32 v189, v214, v215
	v_pk_max_f16 v188, v188, 0
	v_pk_max_f16 v189, v189, 0
	s_waitcnt lgkmcnt(0)
	v_mfma_f32_16x16x32_f16 v[252:255], v[244:247], v[236:239], v[252:255]
	ds_read_u16 v102, v114
	ds_read_u16 v103, v114 offset:512
	ds_read_u16 v115, v114 offset:1024
	ds_read_u16 v116, v114 offset:1536
	v_cvt_pk_f16_f32 v234, v224, v225
	v_cvt_pk_f16_f32 v235, v226, v227
	v_pk_max_f16 v234, v234, 0
	v_pk_max_f16 v235, v235, 0
	v_mfma_f32_16x16x32_f16 v[160:163], v[220:223], v[196:199], v[160:163]
	v_cvt_pk_f16_f32 v190, v204, v205
	v_cvt_pk_f16_f32 v191, v206, v207
	v_pk_max_f16 v190, v190, 0
	v_pk_max_f16 v191, v191, 0
	v_mfma_f32_16x16x32_f16 v[192:195], v[240:243], v[180:183], 0
	v_cvt_pk_f16_f32 v236, v228, v229
	v_cvt_pk_f16_f32 v237, v230, v231
	v_pk_max_f16 v236, v236, 0
	v_pk_max_f16 v237, v237, 0
	v_mfma_f32_16x16x32_f16 v[192:195], v[244:247], v[188:191], v[192:195]
	v_cvt_pk_f16_f32 v238, v216, v217
	v_cvt_pk_f16_f32 v239, v218, v219
	v_pk_max_f16 v238, v238, 0
	v_pk_max_f16 v239, v239, 0
	v_cvt_pk_f16_f32 v180, v200, v201
	v_cvt_pk_f16_f32 v181, v202, v203
	v_pk_max_f16 v180, v180, 0
	v_pk_max_f16 v181, v181, 0
	v_mfma_f32_16x16x32_f16 v[196:199], v[240:243], v[232:235], 0
	v_cvt_pk_f16_f32 v182, v136, v137
	v_cvt_pk_f16_f32 v183, v138, v139
	v_pk_max_f16 v182, v182, 0
	v_pk_max_f16 v183, v183, 0
	v_mfma_f32_16x16x32_f16 v[196:199], v[244:247], v[236:239], v[196:199]
	v_cvt_pk_f16_f32 v188, v184, v185
	v_cvt_pk_f16_f32 v189, v186, v187
	v_pk_max_f16 v188, v188, 0
	v_pk_max_f16 v189, v189, 0
	v_cvt_pk_f16_f32 v190, v160, v161
	v_cvt_pk_f16_f32 v191, v162, v163
	v_pk_max_f16 v190, v190, 0
	v_pk_max_f16 v191, v191, 0
	v_mfma_f32_16x16x32_f16 v[122:125], v[240:243], v[180:183], 0
	s_nop 0
	v_mfma_f32_16x16x32_f16 v[122:125], v[244:247], v[188:191], v[122:125]
	v_add_u32_e32 v117, 0x12c00, v105
	v_cndmask_b32_e64 v0, v252, v192, s[2:3]
	v_cndmask_b32_e64 v0, v0, v196, s[0:1]
	s_waitcnt vmcnt(16)
	v_cndmask_b32_e64 v1, v30, v134, s[0:1]
	v_bfi_b32 v30, s10, v1, v30
	v_perm_b32 v1, v22, v134, s24
	v_cndmask_b32_e64 v22, v22, v1, s[0:1]
	v_cndmask_b32_e64 v0, v0, v122, s[26:27]
	ds_write_b32 v112, v0
	v_bfi_b32 v1, s10, v135, v18
	v_perm_b32 v121, v10, v135, s24
	v_cndmask_b32_e64 v18, v18, v1, s[0:1]
	v_cndmask_b32_e64 v10, v10, v121, s[0:1]
	s_add_i32 s22, s22, 0x80000
	s_add_i32 s11, s11, 1
	s_add_u32 s12, s12, 4
	s_addc_u32 s13, s13, 0
	v_add_u32_e32 v104, 0x400, v104
	v_add_u32_e32 v105, 0x800, v105
	v_add_u32_e32 v114, 2, v114
	s_cmp_eq_u32 s22, 0x898000
	s_waitcnt lgkmcnt(0)
	s_barrier
	ds_read_b128 v[232:235], v113
	ds_read_b128 v[236:239], v113 offset:1024
	s_waitcnt lgkmcnt(0)
	v_add_f32_e32 v0, v232, v233
	v_add_f32_e32 v1, v234, v235
	v_add_f32_e32 v121, v236, v237
	v_add_f32_e32 v144, v238, v239
	v_add_f32_e32 v0, v0, v1
	v_add_f32_e32 v121, v121, v144
	v_add_f32_e32 v0, v0, v121
	v_add_f32_e32 v0, s30, v0
	v_cvt_f16_f32_e32 v1, v0
	v_cvt_f16_f32_e32 v121, v0
	ds_write_b32 v106, v0
	v_add_u32_e32 v106, 4, v106
	v_permlane16_swap_b32_e32 v1, v121
	s_cbranch_scc0 .LBB1_4
